# tail: all 4 tokens of a 32-token tile (both loop iterations) loaded at the tile header together with the per-tile parameter vectors; dropped 4 leftover store-only waits
# speedup vs baseline: 1.0008x; 1.0008x over previous
; DI void phase_tail(const Frame& F, int l) {
;     ...
;     for (int ti = F.vcu; ti < T / 32; ti += F.G) {
;         f32x4 Bv[4], Av[4], Sv[4];
;         { const int b = (32 * ti) / SEQ; const float* m = MOD + ((size_t)l * NB + b) * 6144; f32x4 g[4], c[4];
;           load_vec(F.ap->in[5] + (size_t)l * D, F.lane, g); load_vec(m + 2 * D, F.lane, c);
; #pragma unroll
;           for (int j = 0; j < 4; ++j) Bv[j] = g[j] * c[j];
;           load_vec(F.ap->in[6] + (size_t)l * D, F.lane, g); load_vec(m + 4 * D, F.lane, c); load_vec(m + 3 * D, F.lane, Sv);
; #pragma unroll
;           for (int j = 0; j < 4; ++j) Av[j] = g[j] * (c[j] + 1.f); }
; #pragma unroll 2
;         for (int q = 0; q < 4; ++q) {
;             const int tkl = 4 * F.wave + q, t = 32 * ti + tkl;
;             f32x4 y[4], x[4], hv[4];
;             load_bf16_row((const bf16_t*)(F.ws + WS_Y) + (size_t)t * D, F.lane, y);
;     ...
;             const int tkl = 4 * F.wave + 2 * it + h, t = 32 * ti + tkl;
.LBB0_959:
	s_ashr_i32 s2, s24, 31
	s_ashr_i32 s65, s64, 31
	s_lshr_b32 s2, s2, 25
	s_lshl_b64 s[4:5], s[64:65], 11
	s_add_i32 s2, s24, s2
	v_mov_b32_e32 v63, s5
	v_or_b32_e32 v62, s4, v52
	s_lshl_b64 s[4:5], s[64:65], 10
	s_ashr_i32 s2, s2, 7
	v_or_b32_e32 v64, s4, v192
	s_ashr_i32 s4, s2, 31
	s_add_u32 s2, s48, s2
	s_addc_u32 s4, s49, s4
	v_mov_b32_e32 v65, s5
	s_mulk_i32 s4, 0x6000
	s_mul_hi_u32 s5, s2, 0x6000
	s_add_i32 s5, s5, s4
	s_mulk_i32 s2, 0x6000
	s_add_u32 s2, s9, s2
	s_addc_u32 s6, s19, s5
	s_add_u32 s4, s2, 0x2000
	s_addc_u32 s5, s6, 0
	v_lshlrev_b32_e32 v132, 2, v192
	global_load_dwordx4 v[148:151], v[48:49], off offset:16
	global_load_dwordx4 v[152:155], v[48:49], off
	s_waitcnt lgkmcnt(0)
	global_load_dwordx4 v[176:179], v[48:49], off offset:2064
	global_load_dwordx4 v[180:183], v[48:49], off offset:2048
	global_load_dwordx4 v[74:77], v132, s[4:5] offset:16
	global_load_dwordx4 v[70:73], v132, s[4:5]
	global_load_dwordx4 v[82:85], v140, s[4:5] offset:16
	global_load_dwordx4 v[78:81], v140, s[4:5]
	s_add_u32 s4, s2, 0x4000
	s_addc_u32 s5, s6, 0
	global_load_dwordx4 v[90:93], v[50:51], off offset:16
	global_load_dwordx4 v[86:89], v[50:51], off
	global_load_dwordx4 v[98:101], v[50:51], off offset:2064
	global_load_dwordx4 v[94:97], v[50:51], off offset:2048
	global_load_dwordx4 v[102:105], v132, s[4:5] offset:16
	global_load_dwordx4 v[106:109], v132, s[4:5]
	global_load_dwordx4 v[128:131], v140, s[4:5] offset:16
	global_load_dwordx4 v[114:117], v140, s[4:5]
	s_add_u32 s4, s2, 0x3000
	s_addc_u32 s5, s6, 0
	s_mov_b32 s46, s22
	global_load_dwordx4 v[0:3], v132, s[4:5] offset:16
	global_load_dwordx4 v[4:7], v132, s[4:5]
	global_load_dwordx4 v[8:11], v140, s[4:5] offset:16
	global_load_dwordx4 v[12:15], v140, s[4:5]
	s_brev_b32 s25, 23
	v_lshl_add_u64 v[242:243], s[54:55], 0, v[62:63]
	v_add_co_u32_e32 v250, vcc, 0x94000000, v242
	s_nop 0
	v_addc_co_u32_e32 v251, vcc, 0, v243, vcc
	v_add_co_u32_e32 v212, vcc, s25, v242
	global_load_dwordx4 v[124:127], v[250:251], off
	global_load_dwordx4 v[144:147], v[250:251], off offset:1024
	v_addc_co_u32_e32 v213, vcc, 0, v243, vcc
	global_load_dwordx4 v[110:113], v[212:213], off
	global_load_dwordx4 v[118:121], v[212:213], off offset:1024
	s_ashr_i32 s47, s46, 31
	s_lshl_b64 s[12:13], s[46:47], 11
	v_lshl_add_u64 v[214:215], v[54:55], 0, s[12:13]
	v_lshl_add_u64 v[216:217], v[56:57], 0, s[12:13]
	global_load_dwordx4 v[160:163], v[214:215], off
	global_load_dwordx4 v[164:167], v[214:215], off offset:1024
	global_load_dwordx4 v[168:171], v[216:217], off
	global_load_dwordx4 v[172:175], v[216:217], off offset:1024
	v_lshl_add_u64 v[242:243], v[242:243], 0, s[0:1]
	v_add_co_u32_e32 v250, vcc, 0x94000000, v242
	s_nop 0
	v_addc_co_u32_e32 v251, vcc, 0, v243, vcc
	v_add_co_u32_e32 v212, vcc, s25, v242
	global_load_dwordx4 v[194:197], v[250:251], off
	global_load_dwordx4 v[198:201], v[250:251], off offset:1024
	v_addc_co_u32_e32 v213, vcc, 0, v243, vcc
	global_load_dwordx4 v[202:205], v[212:213], off
	global_load_dwordx4 v[226:229], v[212:213], off offset:1024
	s_add_i32 s12, s46, 2
	s_ashr_i32 s13, s12, 31
	s_lshl_b64 s[12:13], s[12:13], 11
	v_lshl_add_u64 v[214:215], v[54:55], 0, s[12:13]
	v_lshl_add_u64 v[216:217], v[56:57], 0, s[12:13]
	global_load_dwordx4 v[230:233], v[214:215], off
	global_load_dwordx4 v[234:237], v[214:215], off offset:1024
	global_load_dwordx4 v[238:241], v[216:217], off
	global_load_dwordx4 v[246:249], v[216:217], off offset:1024
	s_waitcnt vmcnt(31)
	v_pk_mul_f32 v[74:75], v[148:149], v[74:75]
	s_waitcnt vmcnt(30)
	v_pk_mul_f32 v[68:69], v[154:155], v[72:73]
	v_pk_mul_f32 v[70:71], v[152:153], v[70:71]
	v_pk_mul_f32 v[72:73], v[150:151], v[76:77]
	s_waitcnt vmcnt(28)
	v_pk_mul_f32 v[76:77], v[182:183], v[80:81]
	v_pk_mul_f32 v[78:79], v[180:181], v[78:79]
	v_pk_mul_f32 v[80:81], v[178:179], v[84:85]
	v_pk_mul_f32 v[82:83], v[176:177], v[82:83]
	s_waitcnt vmcnt(22)
	v_pk_add_f32 v[84:85], v[108:109], 1.0 op_sel_hi:[1,0]
	v_pk_add_f32 v[102:103], v[102:103], 1.0 op_sel_hi:[1,0]
	v_pk_mul_f32 v[84:85], v[88:89], v[84:85]
	v_pk_add_f32 v[88:89], v[104:105], 1.0 op_sel_hi:[1,0]
	v_pk_mul_f32 v[90:91], v[90:91], v[102:103]
	v_pk_mul_f32 v[88:89], v[92:93], v[88:89]
	s_waitcnt vmcnt(20)
	v_pk_add_f32 v[92:93], v[116:117], 1.0 op_sel_hi:[1,0]
	v_pk_add_f32 v[102:103], v[114:115], 1.0 op_sel_hi:[1,0]
	v_pk_add_f32 v[106:107], v[106:107], 1.0 op_sel_hi:[1,0]
	v_pk_mul_f32 v[92:93], v[96:97], v[92:93]
	v_pk_mul_f32 v[94:95], v[94:95], v[102:103]
	v_pk_add_f32 v[96:97], v[130:131], 1.0 op_sel_hi:[1,0]
	v_pk_add_f32 v[102:103], v[128:129], 1.0 op_sel_hi:[1,0]
	v_pk_mul_f32 v[86:87], v[86:87], v[106:107]
	v_pk_mul_f32 v[96:97], v[100:101], v[96:97]
	v_pk_mul_f32 v[98:99], v[98:99], v[102:103]
	s_mov_b32 s4, 0
.LBB0_960:
	s_cmp_eq_u32 s4, 0
	s_cbranch_scc1 .Ltail_pf_it0
	s_waitcnt vmcnt(8)
	v_mov_b32_e32 v124, v194
	v_mov_b32_e32 v125, v195
	v_mov_b32_e32 v126, v196
	v_mov_b32_e32 v127, v197
	v_mov_b32_e32 v144, v198
	v_mov_b32_e32 v145, v199
	v_mov_b32_e32 v146, v200
	v_mov_b32_e32 v147, v201
	v_mov_b32_e32 v110, v202
	v_mov_b32_e32 v111, v203
	v_mov_b32_e32 v112, v204
	v_mov_b32_e32 v113, v205
	v_mov_b32_e32 v118, v226
	v_mov_b32_e32 v119, v227
	v_mov_b32_e32 v120, v228
	v_mov_b32_e32 v121, v229
	v_mov_b32_e32 v160, v230
	v_mov_b32_e32 v161, v231
	v_mov_b32_e32 v162, v232
	v_mov_b32_e32 v163, v233
	v_mov_b32_e32 v164, v234
	v_mov_b32_e32 v165, v235
	v_mov_b32_e32 v166, v236
	v_mov_b32_e32 v167, v237
	v_mov_b32_e32 v168, v238
	v_mov_b32_e32 v169, v239
	v_mov_b32_e32 v170, v240
	v_mov_b32_e32 v171, v241
	v_mov_b32_e32 v172, v246
	v_mov_b32_e32 v173, v247
	v_mov_b32_e32 v174, v248
	v_mov_b32_e32 v175, v249
; DI void phase_tail(const Frame& F, int l) {
;     ...
;             load_bf16_row((const bf16_t*)(F.ws + WS_Y) + (size_t)t * D, F.lane, y);
;             load_bf16_row((const bf16_t*)(F.ws + WS_XB) + (size_t)t * D, F.lane, x);
;             const float rstd = rms_rstd(y);
; #pragma unroll
;             for (int j = 0; j < 4; ++j) x[j] = x[j] + Bv[j] * (y[j] * rstd);
;             store_bf16_row((bf16_t*)(F.ws + WS_XB) + (size_t)t * D, F.lane, x);
.Ltail_pf_it0:
	v_lshl_add_u64 v[100:101], s[54:55], 0, v[62:63]
	v_add_co_u32_e32 v102, vcc, 0x94000000, v100
	s_brev_b32 s2, 23
	s_nop 0
	v_addc_co_u32_e32 v103, vcc, 0, v101, vcc
	v_add_co_u32_e32 v116, vcc, s2, v100
	v_addc_co_u32_e32 v117, vcc, 0, v101, vcc
	s_ashr_i32 s47, s46, 31
	s_lshl_b64 s[66:67], s[46:47], 10
	s_lshl_b64 s[68:69], s[46:47], 11
	v_lshl_add_u64 v[176:177], v[54:55], 0, s[68:69]
	v_lshl_add_u64 v[178:179], v[56:57], 0, s[68:69]
	v_lshl_add_u64 v[62:63], v[62:63], 0, s[0:1]
	s_waitcnt vmcnt(15)
	v_lshlrev_b32_e32 v128, 16, v125
	s_waitcnt vmcnt(14)
	v_lshlrev_b32_e32 v108, 16, v146
	v_and_b32_e32 v143, 0xffff0000, v146
	v_lshlrev_b32_e32 v114, 16, v147
	s_waitcnt vmcnt(13)
	v_lshlrev_b32_e32 v102, 16, v110
	v_and_b32_e32 v103, 0xffff0000, v110
	v_lshlrev_b32_e32 v110, 16, v124
	v_lshlrev_b32_e32 v100, 16, v111
	v_and_b32_e32 v101, 0xffff0000, v111
	v_and_b32_e32 v111, 0xffff0000, v124
	v_mul_f32_e32 v124, v110, v110
	v_and_b32_e32 v115, 0xffff0000, v147
	v_pk_fma_f32 v[146:147], v[110:111], v[110:111], v[124:125] op_sel_hi:[1,1,0]
	v_and_b32_e32 v129, 0xffff0000, v125
	v_mul_f32_e32 v124, v128, v128
	v_pk_fma_f32 v[148:149], v[128:129], v[128:129], v[124:125] op_sel_hi:[1,1,0]
	v_lshlrev_b32_e32 v125, 16, v127
	v_lshlrev_b32_e32 v124, 16, v126
	v_and_b32_e32 v127, 0xffff0000, v127
	v_and_b32_e32 v126, 0xffff0000, v126
	v_pk_mul_f32 v[130:131], v[126:127], v[126:127]
	v_mov_b32_e32 v109, v147
	v_pk_fma_f32 v[130:131], v[124:125], v[124:125], v[130:131]
	v_mov_b32_e32 v154, v108
	v_pk_add_f32 v[150:151], v[130:131], v[130:131] op_sel_hi:[0,1]
	v_lshlrev_b32_e32 v130, 16, v144
	v_and_b32_e32 v131, 0xffff0000, v144
	v_mul_f32_e32 v132, v130, v130
	v_pk_fma_f32 v[152:153], v[130:131], v[130:131], v[132:133] op_sel_hi:[1,1,0]
	v_lshlrev_b32_e32 v132, 16, v145
	v_and_b32_e32 v133, 0xffff0000, v145
	v_mul_f32_e32 v144, v132, v132
	v_mov_b32_e32 v155, v149
	v_pk_fma_f32 v[144:145], v[132:133], v[132:133], v[144:145] op_sel_hi:[1,1,0]
	v_pk_mul_f32 v[154:155], v[108:109], v[154:155]
	v_pk_add_f32 v[146:147], v[146:147], v[148:149]
	v_mul_f32_e32 v150, v143, v143
	v_mul_f32_e32 v152, v114, v114
	v_mul_f32_e32 v144, v115, v115
	v_mov_b32_e32 v155, v147
	v_pk_add_f32 v[146:147], v[154:155], v[150:151]
	v_pk_add_f32 v[144:145], v[152:153], v[144:145]
	v_lshlrev_b32_e32 v106, 16, v112
	v_pk_add_f32 v[144:145], v[146:147], v[144:145]
	v_and_b32_e32 v107, 0xffff0000, v112
	v_add_f32_e32 v109, v144, v145
	s_waitcnt vmcnt(12)
	v_lshlrev_b32_e32 v122, 16, v119
	v_and_b32_e32 v123, 0xffff0000, v119
	v_add_f32_dpp v109, v109, v109 quad_perm:[1,0,3,2] row_mask:0xf bank_mask:0xf bound_ctrl:1
	v_lshlrev_b32_e32 v104, 16, v113
	v_and_b32_e32 v105, 0xffff0000, v113
	v_add_f32_dpp v109, v109, v109 quad_perm:[2,3,0,1] row_mask:0xf bank_mask:0xf bound_ctrl:1
	v_lshlrev_b32_e32 v112, 16, v118
	v_and_b32_e32 v113, 0xffff0000, v118
	v_add_f32_dpp v109, v109, v109 row_half_mirror row_mask:0xf bank_mask:0xf bound_ctrl:1
	v_lshlrev_b32_e32 v118, 16, v120
	v_and_b32_e32 v119, 0xffff0000, v120
	v_add_f32_dpp v109, v109, v109 row_mirror row_mask:0xf bank_mask:0xf bound_ctrl:1
	v_lshlrev_b32_e32 v120, 16, v121
	v_readlane_b32 s2, v109, 16
	v_readlane_b32 s5, v109, 48
	v_readlane_b32 s6, v109, 0
	v_readlane_b32 s7, v109, 32
	v_mov_b32_e32 v144, s2
	v_mov_b32_e32 v145, s5
	v_pk_add_f32 v[144:145], s[6:7], v[144:145]
	v_and_b32_e32 v121, 0xffff0000, v121
	v_add_f32_e32 v109, v144, v145
	v_mov_b32_e32 v144, 0x358637bd
	s_nop 0
	v_fmac_f32_e32 v144, 0x3a800000, v109
	v_rsq_f32_e32 v144, v144
	v_mov_b32_e32 v109, v143
	v_add_u32_e32 v143, s4, v139
	s_addk_i32 s4, 0x1020
	v_pk_mul_f32 v[110:111], v[144:145], v[110:111] op_sel_hi:[0,1]
	v_pk_fma_f32 v[102:103], v[70:71], v[110:111], v[102:103]
	v_mov_b32_e32 v110, v124
	v_mov_b32_e32 v111, v126
	v_pk_mul_f32 v[110:111], v[144:145], v[110:111] op_sel_hi:[0,1]
	v_pk_fma_f32 v[110:111], v[74:75], v[110:111], v[106:107]
	v_pk_mul_f32 v[106:107], v[144:145], v[132:133] op_sel_hi:[0,1]
	v_pk_fma_f32 v[106:107], v[76:77], v[106:107], v[122:123]
	v_pk_mul_f32 v[122:123], v[108:109], v[144:145] op_sel_hi:[1,0]
	v_pk_mul_f32 v[108:109], v[114:115], v[144:145] op_sel_hi:[1,0]
	v_pk_fma_f32 v[114:115], v[82:83], v[122:123], v[118:119]
	v_bfe_u32 v118, v102, 16, 1
	v_pk_mul_f32 v[128:129], v[144:145], v[128:129] op_sel_hi:[0,1]
	v_add3_u32 v118, v102, v118, s15
	v_bfe_u32 v119, v103, 16, 1
	v_pk_fma_f32 v[100:101], v[68:69], v[128:129], v[100:101]
	v_lshrrev_b32_e32 v118, 16, v118
	v_add3_u32 v119, v103, v119, s15
	v_and_or_b32 v118, v119, s16, v118
	v_bfe_u32 v119, v100, 16, 1
	v_pk_fma_f32 v[108:109], v[80:81], v[108:109], v[120:121]
	v_add3_u32 v119, v100, v119, s15
	v_bfe_u32 v120, v101, 16, 1
	v_lshrrev_b32_e32 v119, 16, v119
	v_add3_u32 v120, v101, v120, s15
	v_mov_b32_e32 v126, v125
	v_and_or_b32 v119, v120, s16, v119
	v_bfe_u32 v120, v110, 16, 1
	v_pk_mul_f32 v[124:125], v[144:145], v[126:127] op_sel_hi:[0,1]
	v_add3_u32 v120, v110, v120, s15
	v_bfe_u32 v121, v111, 16, 1
	v_pk_fma_f32 v[104:105], v[72:73], v[124:125], v[104:105]
	v_lshrrev_b32_e32 v120, 16, v120
	v_add3_u32 v121, v111, v121, s15
	v_and_or_b32 v120, v121, s16, v120
	v_bfe_u32 v121, v104, 16, 1
	v_add3_u32 v121, v104, v121, s15
	v_bfe_u32 v122, v105, 16, 1
	v_pk_mul_f32 v[124:125], v[144:145], v[130:131] op_sel_hi:[0,1]
	v_lshrrev_b32_e32 v121, 16, v121
	v_add3_u32 v122, v105, v122, s15
	v_pk_fma_f32 v[112:113], v[78:79], v[124:125], v[112:113]
	v_and_or_b32 v121, v122, s16, v121
	global_store_dwordx4 v[116:117], v[118:121], off
	v_bfe_u32 v122, v109, 16, 1
	v_add3_u32 v122, v109, v122, s15
	v_bfe_u32 v118, v112, 16, 1
	v_add3_u32 v118, v112, v118, s15
; #define LAS __attribute__((address_space(3)))
; DI unsigned pk2(float lo, float hi) { return f2bf(lo) | (f2bf(hi) << 16); }
; DI unsigned pk_fp8x4(float a, float b, float c, float d) { int p = 0; p = __builtin_amdgcn_cvt_pk_fp8_f32(a, b, p, false); p = __builtin_amdgcn_cvt_pk_fp8_f32(c, d, p, true); return (unsigned)p; }
; DI void phase_tail(const Frame& F, int l) {
;     ...
;             store_bf16_row((bf16_t*)(F.ws + WS_XB) + (size_t)t * D, F.lane, x);
;             { const float rs2 = rms_rstd(x);
; #pragma unroll
;               for (int j = 0; j < 4; ++j) hv[j] = x[j] * rs2 * Av[j] + Sv[j];
; #pragma unroll
;               for (int g = 0; g < 2; ++g) { u32x2 w; w.x = pk_fp8x4(hv[2 * g].x, hv[2 * g].y, hv[2 * g].z, hv[2 * g].w); w.y = pk_fp8x4(hv[2 * g + 1].x, hv[2 * g + 1].y, hv[2 * g + 1].z, hv[2 * g + 1].w);
;                   *(u32x2*)((unsigned char*)(F.ws + WS_H8) + (size_t)t * D + 8 * F.lane + 512 * g) = w; } }
; #pragma unroll
;             for (int g = 0; g < 2; ++g) { u32x4 w; w.x = pk2(hv[2 * g].x, hv[2 * g].y); w.y = pk2(hv[2 * g].z, hv[2 * g].w); w.z = pk2(hv[2 * g + 1].x, hv[2 * g + 1].y); w.w = pk2(hv[2 * g + 1].z, hv[2 * g + 1].w);
;                 *(LAS u32x4*)(Ht + tkl * HT_STRIDE + 8 * F.lane + 512 * g) = w; }
	v_bfe_u32 v119, v113, 16, 1
	v_lshrrev_b32_e32 v118, 16, v118
	v_add3_u32 v119, v113, v119, s15
	v_and_or_b32 v118, v119, s16, v118
	v_bfe_u32 v119, v106, 16, 1
	v_add3_u32 v119, v106, v119, s15
	v_bfe_u32 v120, v107, 16, 1
	v_lshrrev_b32_e32 v119, 16, v119
	v_add3_u32 v120, v107, v120, s15
	v_and_or_b32 v119, v120, s16, v119
	v_bfe_u32 v120, v114, 16, 1
	v_add3_u32 v120, v114, v120, s15
	v_bfe_u32 v121, v115, 16, 1
	v_lshrrev_b32_e32 v120, 16, v120
	v_add3_u32 v121, v115, v121, s15
	v_and_or_b32 v120, v121, s16, v120
	v_bfe_u32 v121, v108, 16, 1
	v_add3_u32 v121, v108, v121, s15
	v_lshrrev_b32_e32 v121, 16, v121
	v_and_or_b32 v121, v122, s16, v121
	global_store_dwordx4 v[116:117], v[118:121], off offset:1024
	v_pk_mul_f32 v[116:117], v[100:101], v[100:101]
	s_nop 0
	v_pk_mul_f32 v[118:119], v[102:103], v[102:103]
	s_nop 0
	v_pk_mov_b32 v[120:121], v[118:119], v[116:117] op_sel:[1,0]
	v_mov_b32_e32 v119, v117
	v_pk_add_f32 v[116:117], v[120:121], v[118:119]
	v_pk_mul_f32 v[118:119], v[104:105], v[104:105]
	v_pk_add_f32 v[116:117], v[116:117], v[116:117] op_sel_hi:[0,1]
	v_pk_mul_f32 v[120:121], v[110:111], v[110:111]
	v_mul_f32_e32 v116, v112, v112
	v_pk_mov_b32 v[122:123], v[120:121], v[118:119] op_sel:[1,0]
	v_mov_b32_e32 v121, v119
	v_pk_add_f32 v[118:119], v[122:123], v[120:121]
	v_pk_fma_f32 v[120:121], v[112:113], v[112:113], v[116:117] op_sel_hi:[1,1,0]
	v_mul_f32_e32 v116, v106, v106
	v_pk_add_f32 v[118:119], v[118:119], v[118:119] op_sel_hi:[0,1]
	v_pk_fma_f32 v[122:123], v[106:107], v[106:107], v[116:117] op_sel_hi:[1,1,0]
	v_mul_f32_e32 v120, v114, v114
	v_mul_f32_e32 v122, v115, v115
	v_mul_f32_e32 v116, v108, v108
	v_mul_f32_e32 v118, v109, v109
	v_pk_add_f32 v[120:121], v[120:121], v[122:123]
	v_pk_add_f32 v[116:117], v[116:117], v[118:119]
	s_nop 0
	v_pk_add_f32 v[116:117], v[120:121], v[116:117]
	s_nop 0
	v_add_f32_e32 v116, v116, v117
	s_nop 1
	v_add_f32_dpp v116, v116, v116 quad_perm:[1,0,3,2] row_mask:0xf bank_mask:0xf bound_ctrl:1
	s_nop 1
	v_add_f32_dpp v116, v116, v116 quad_perm:[2,3,0,1] row_mask:0xf bank_mask:0xf bound_ctrl:1
	s_nop 1
	v_add_f32_dpp v116, v116, v116 row_half_mirror row_mask:0xf bank_mask:0xf bound_ctrl:1
	s_nop 1
	v_add_f32_dpp v116, v116, v116 row_mirror row_mask:0xf bank_mask:0xf bound_ctrl:1
	s_nop 0
	v_readlane_b32 s2, v116, 16
	v_readlane_b32 s5, v116, 48
	v_readlane_b32 s6, v116, 0
	v_readlane_b32 s7, v116, 32
	v_mov_b32_e32 v116, s2
	v_mov_b32_e32 v117, s5
	v_pk_add_f32 v[116:117], s[6:7], v[116:117]
	s_lshl_b64 s[6:7], s[46:47], 11
	v_add_f32_e32 v116, v116, v117
	v_mov_b32_e32 v117, 0x358637bd
	s_add_i32 s46, s46, 2
	v_fmac_f32_e32 v117, 0x3a800000, v116
	v_rsq_f32_e32 v116, v117
	s_cmpk_eq_i32 s4, 0x2040
	v_pk_mul_f32 v[100:101], v[100:101], v[116:117] op_sel_hi:[1,0]
	v_pk_mul_f32 v[102:103], v[102:103], v[116:117] op_sel_hi:[1,0]
	v_pk_fma_f32 v[118:119], v[84:85], v[100:101], v[6:7]
	v_pk_mul_f32 v[100:101], v[110:111], v[116:117] op_sel_hi:[1,0]
	v_pk_fma_f32 v[120:121], v[86:87], v[102:103], v[4:5]
	v_pk_mul_f32 v[102:103], v[104:105], v[116:117] op_sel_hi:[1,0]
	v_pk_fma_f32 v[110:111], v[90:91], v[100:101], v[0:1]
	v_pk_mul_f32 v[100:101], v[112:113], v[116:117] op_sel_hi:[1,0]
	v_pk_fma_f32 v[122:123], v[88:89], v[102:103], v[2:3]
	v_pk_mul_f32 v[102:103], v[106:107], v[116:117] op_sel_hi:[1,0]
	v_pk_fma_f32 v[106:107], v[94:95], v[100:101], v[12:13]
	v_pk_mul_f32 v[100:101], v[108:109], v[116:117] op_sel_hi:[1,0]
	v_mov_b32_e32 v108, v193
	v_mov_b32_e32 v109, v193
	v_cvt_pk_fp8_f32 v108, v120, v121
	v_cvt_pk_fp8_f32 v109, v110, v111
	v_lshl_add_u64 v[112:113], s[54:55], 0, v[64:65]
	v_add_co_u32_e32 v112, vcc, s18, v112
	v_cvt_pk_fp8_f32 v108, v118, v119 op_sel:[0,0,1]
	v_cvt_pk_fp8_f32 v109, v122, v123 op_sel:[0,0,1]
	v_pk_fma_f32 v[104:105], v[92:93], v[102:103], v[14:15]
	v_pk_mul_f32 v[102:103], v[114:115], v[116:117] op_sel_hi:[1,0]
	v_addc_co_u32_e32 v113, vcc, 0, v113, vcc
	v_pk_fma_f32 v[102:103], v[98:99], v[102:103], v[8:9]
	global_store_dwordx2 v[112:113], v[108:109], off
	v_mov_b32_e32 v108, v193
	v_mov_b32_e32 v109, v193
	v_cvt_pk_fp8_f32 v108, v106, v107
	v_cvt_pk_fp8_f32 v109, v102, v103
	v_pk_fma_f32 v[100:101], v[96:97], v[100:101], v[10:11]
	v_lshl_add_u64 v[116:117], v[56:57], 0, s[6:7]
	v_cvt_pk_fp8_f32 v108, v104, v105 op_sel:[0,0,1]
	v_cvt_pk_fp8_f32 v109, v100, v101 op_sel:[0,0,1]
	v_lshl_add_u64 v[64:65], v[64:65], 0, s[34:35]
	global_store_dwordx2 v[112:113], v[108:109], off offset:512
	v_bfe_u32 v108, v120, 16, 1
	v_add3_u32 v108, v120, v108, s15
	v_bfe_u32 v109, v121, 16, 1
	v_lshrrev_b32_e32 v108, 16, v108
	v_add3_u32 v109, v121, v109, s15
	v_and_or_b32 v108, v109, s16, v108
	v_bfe_u32 v109, v118, 16, 1
	v_add3_u32 v109, v118, v109, s15
	v_bfe_u32 v112, v119, 16, 1
	v_lshrrev_b32_e32 v109, 16, v109
	v_add3_u32 v112, v119, v112, s15
	v_and_or_b32 v109, v112, s16, v109
	v_bfe_u32 v112, v110, 16, 1
	v_add3_u32 v110, v110, v112, s15
	v_bfe_u32 v112, v111, 16, 1
	v_lshrrev_b32_e32 v110, 16, v110
	v_add3_u32 v111, v111, v112, s15
	v_and_or_b32 v110, v111, s16, v110
	v_bfe_u32 v111, v122, 16, 1
	v_add3_u32 v111, v122, v111, s15
	v_bfe_u32 v112, v123, 16, 1
	v_lshrrev_b32_e32 v111, 16, v111
	v_add3_u32 v112, v123, v112, s15
	v_and_or_b32 v111, v112, s16, v111
	ds_write_b128 v143, v[108:111]
	v_bfe_u32 v108, v106, 16, 1
	v_add3_u32 v106, v106, v108, s15
	v_bfe_u32 v108, v107, 16, 1
	v_lshrrev_b32_e32 v106, 16, v106
	v_add3_u32 v107, v107, v108, s15
	v_and_or_b32 v106, v107, s16, v106
	v_bfe_u32 v107, v104, 16, 1
	v_add3_u32 v104, v104, v107, s15
	v_bfe_u32 v107, v105, 16, 1
	v_lshrrev_b32_e32 v104, 16, v104
	v_add3_u32 v105, v105, v107, s15
	v_and_or_b32 v107, v105, s16, v104
	v_bfe_u32 v104, v102, 16, 1
	v_add3_u32 v102, v102, v104, s15
	v_bfe_u32 v104, v103, 16, 1
	v_lshrrev_b32_e32 v102, 16, v102
	v_add3_u32 v103, v103, v104, s15
	v_and_or_b32 v108, v103, s16, v102
	v_bfe_u32 v102, v100, 16, 1
	v_add3_u32 v100, v100, v102, s15
	v_bfe_u32 v102, v101, 16, 1
	v_lshrrev_b32_e32 v100, 16, v100
	v_add3_u32 v101, v101, v102, s15
	v_and_or_b32 v109, v101, s16, v100
	ds_write_b128 v143, v[106:109] offset:1024
	v_lshl_add_u64 v[100:101], v[54:55], 0, s[6:7]
	s_waitcnt vmcnt(12)
; DI void phase_tail(const Frame& F, int l) {
;     ...
;             load_bf16_row((const bf16_t*)(F.ws + WS_Y) + (size_t)t * D, F.lane, y);
;             load_bf16_row((const bf16_t*)(F.ws + WS_XB) + (size_t)t * D, F.lane, x);
;             const float rstd = rms_rstd(y);
; #pragma unroll
;             for (int j = 0; j < 4; ++j) x[j] = x[j] + Bv[j] * (y[j] * rstd);
;             store_bf16_row((bf16_t*)(F.ws + WS_XB) + (size_t)t * D, F.lane, x);
	v_mov_b32_e32 v124, v160
	v_mov_b32_e32 v125, v161
	v_mov_b32_e32 v126, v162
	v_mov_b32_e32 v127, v163
	v_mov_b32_e32 v144, v164
	v_mov_b32_e32 v145, v165
	v_mov_b32_e32 v146, v166
	v_mov_b32_e32 v147, v167
	v_mov_b32_e32 v110, v168
	v_mov_b32_e32 v111, v169
	v_mov_b32_e32 v112, v170
	v_mov_b32_e32 v113, v171
	v_mov_b32_e32 v118, v172
	v_mov_b32_e32 v119, v173
	v_mov_b32_e32 v120, v174
	v_mov_b32_e32 v121, v175
	v_lshlrev_b32_e32 v128, 16, v125
	v_lshlrev_b32_e32 v108, 16, v146
	v_lshlrev_b32_e32 v102, 16, v110
	v_and_b32_e32 v103, 0xffff0000, v110
	v_lshlrev_b32_e32 v110, 16, v124
	v_lshlrev_b32_e32 v100, 16, v111
	v_and_b32_e32 v101, 0xffff0000, v111
	v_and_b32_e32 v111, 0xffff0000, v124
	v_mul_f32_e32 v124, v110, v110
	v_and_b32_e32 v156, 0xffff0000, v146
	v_lshlrev_b32_e32 v114, 16, v147
	v_and_b32_e32 v115, 0xffff0000, v147
	v_pk_fma_f32 v[146:147], v[110:111], v[110:111], v[124:125] op_sel_hi:[1,1,0]
	v_and_b32_e32 v129, 0xffff0000, v125
	v_mul_f32_e32 v124, v128, v128
	v_pk_fma_f32 v[148:149], v[128:129], v[128:129], v[124:125] op_sel_hi:[1,1,0]
	v_lshlrev_b32_e32 v125, 16, v127
	v_lshlrev_b32_e32 v124, 16, v126
	v_and_b32_e32 v127, 0xffff0000, v127
	v_and_b32_e32 v126, 0xffff0000, v126
	v_pk_mul_f32 v[130:131], v[126:127], v[126:127]
	v_mov_b32_e32 v109, v147
	v_pk_fma_f32 v[130:131], v[124:125], v[124:125], v[130:131]
	v_mov_b32_e32 v154, v108
	v_pk_add_f32 v[150:151], v[130:131], v[130:131] op_sel_hi:[0,1]
	v_lshlrev_b32_e32 v130, 16, v144
	v_and_b32_e32 v131, 0xffff0000, v144
	v_mul_f32_e32 v132, v130, v130
	v_pk_fma_f32 v[152:153], v[130:131], v[130:131], v[132:133] op_sel_hi:[1,1,0]
	v_lshlrev_b32_e32 v132, 16, v145
	v_and_b32_e32 v133, 0xffff0000, v145
	v_mul_f32_e32 v144, v132, v132
	v_mov_b32_e32 v155, v149
	v_pk_fma_f32 v[144:145], v[132:133], v[132:133], v[144:145] op_sel_hi:[1,1,0]
	v_pk_mul_f32 v[154:155], v[108:109], v[154:155]
	v_pk_add_f32 v[146:147], v[146:147], v[148:149]
	v_mul_f32_e32 v150, v156, v156
	v_mul_f32_e32 v152, v114, v114
	v_mul_f32_e32 v144, v115, v115
	v_mov_b32_e32 v155, v147
	v_pk_add_f32 v[146:147], v[154:155], v[150:151]
	v_pk_add_f32 v[144:145], v[152:153], v[144:145]
	v_lshlrev_b32_e32 v106, 16, v112
	v_pk_add_f32 v[144:145], v[146:147], v[144:145]
	v_and_b32_e32 v107, 0xffff0000, v112
	v_add_f32_e32 v109, v144, v145
	v_lshlrev_b32_e32 v122, 16, v119
	v_and_b32_e32 v123, 0xffff0000, v119
	v_add_f32_dpp v109, v109, v109 quad_perm:[1,0,3,2] row_mask:0xf bank_mask:0xf bound_ctrl:1
	v_lshlrev_b32_e32 v104, 16, v113
	v_and_b32_e32 v105, 0xffff0000, v113
	v_add_f32_dpp v109, v109, v109 quad_perm:[2,3,0,1] row_mask:0xf bank_mask:0xf bound_ctrl:1
	v_lshlrev_b32_e32 v112, 16, v118
	v_and_b32_e32 v113, 0xffff0000, v118
	v_add_f32_dpp v109, v109, v109 row_half_mirror row_mask:0xf bank_mask:0xf bound_ctrl:1
	v_lshlrev_b32_e32 v118, 16, v120
	v_and_b32_e32 v119, 0xffff0000, v120
	v_add_f32_dpp v109, v109, v109 row_mirror row_mask:0xf bank_mask:0xf bound_ctrl:1
	v_lshlrev_b32_e32 v120, 16, v121
	v_readlane_b32 s2, v109, 16
	v_readlane_b32 s5, v109, 48
	v_readlane_b32 s6, v109, 0
	v_readlane_b32 s7, v109, 32
	v_mov_b32_e32 v144, s2
	v_mov_b32_e32 v145, s5
	v_pk_add_f32 v[144:145], s[6:7], v[144:145]
	v_and_b32_e32 v121, 0xffff0000, v121
	v_add_f32_e32 v109, v144, v145
	v_mov_b32_e32 v144, 0x358637bd
	s_nop 0
	v_fmac_f32_e32 v144, 0x3a800000, v109
	v_rsq_f32_e32 v144, v144
	v_mov_b32_e32 v109, v156
	v_pk_mul_f32 v[110:111], v[144:145], v[110:111] op_sel_hi:[0,1]
	v_pk_fma_f32 v[102:103], v[70:71], v[110:111], v[102:103]
	v_mov_b32_e32 v110, v124
	v_mov_b32_e32 v111, v126
	v_pk_mul_f32 v[110:111], v[144:145], v[110:111] op_sel_hi:[0,1]
	v_pk_fma_f32 v[110:111], v[74:75], v[110:111], v[106:107]
	v_pk_mul_f32 v[106:107], v[144:145], v[132:133] op_sel_hi:[0,1]
	v_pk_fma_f32 v[106:107], v[76:77], v[106:107], v[122:123]
	v_pk_mul_f32 v[122:123], v[108:109], v[144:145] op_sel_hi:[1,0]
	v_pk_mul_f32 v[108:109], v[114:115], v[144:145] op_sel_hi:[1,0]
	v_pk_fma_f32 v[114:115], v[82:83], v[122:123], v[118:119]
	v_bfe_u32 v118, v102, 16, 1
	v_pk_mul_f32 v[128:129], v[144:145], v[128:129] op_sel_hi:[0,1]
	v_add3_u32 v118, v102, v118, s15
	v_bfe_u32 v119, v103, 16, 1
	v_pk_fma_f32 v[100:101], v[68:69], v[128:129], v[100:101]
	v_lshrrev_b32_e32 v118, 16, v118
	v_add3_u32 v119, v103, v119, s15
	v_and_or_b32 v118, v119, s16, v118
	v_bfe_u32 v119, v100, 16, 1
	v_pk_fma_f32 v[108:109], v[80:81], v[108:109], v[120:121]
	v_add3_u32 v119, v100, v119, s15
	v_bfe_u32 v120, v101, 16, 1
	v_lshrrev_b32_e32 v119, 16, v119
	v_add3_u32 v120, v101, v120, s15
	v_mov_b32_e32 v126, v125
	v_and_or_b32 v119, v120, s16, v119
	v_bfe_u32 v120, v110, 16, 1
	v_pk_mul_f32 v[124:125], v[144:145], v[126:127] op_sel_hi:[0,1]
	v_add3_u32 v120, v110, v120, s15
	v_bfe_u32 v121, v111, 16, 1
	v_pk_fma_f32 v[104:105], v[72:73], v[124:125], v[104:105]
	v_lshrrev_b32_e32 v120, 16, v120
	v_add3_u32 v121, v111, v121, s15
	v_and_or_b32 v120, v121, s16, v120
	v_bfe_u32 v121, v104, 16, 1
	v_add3_u32 v121, v104, v121, s15
	v_bfe_u32 v122, v105, 16, 1
	v_pk_mul_f32 v[124:125], v[144:145], v[130:131] op_sel_hi:[0,1]
	v_lshrrev_b32_e32 v121, 16, v121
	v_add3_u32 v122, v105, v122, s15
	v_pk_fma_f32 v[112:113], v[78:79], v[124:125], v[112:113]
	v_and_or_b32 v121, v122, s16, v121
	global_store_dwordx4 v[116:117], v[118:121], off
	v_bfe_u32 v122, v109, 16, 1
	v_add3_u32 v122, v109, v122, s15
	v_bfe_u32 v118, v112, 16, 1
	v_add3_u32 v118, v112, v118, s15
	v_bfe_u32 v119, v113, 16, 1
	v_lshrrev_b32_e32 v118, 16, v118
	v_add3_u32 v119, v113, v119, s15
	v_and_or_b32 v118, v119, s16, v118
	v_bfe_u32 v119, v106, 16, 1
	v_add3_u32 v119, v106, v119, s15
	v_bfe_u32 v120, v107, 16, 1
; #define LAS __attribute__((address_space(3)))
; DI unsigned pk2(float lo, float hi) { return f2bf(lo) | (f2bf(hi) << 16); }
; DI unsigned pk_fp8x4(float a, float b, float c, float d) { int p = 0; p = __builtin_amdgcn_cvt_pk_fp8_f32(a, b, p, false); p = __builtin_amdgcn_cvt_pk_fp8_f32(c, d, p, true); return (unsigned)p; }
; DI void phase_tail(const Frame& F, int l) {
;     ...
;             store_bf16_row((bf16_t*)(F.ws + WS_XB) + (size_t)t * D, F.lane, x);
;             { const float rs2 = rms_rstd(x);
; #pragma unroll
;               for (int j = 0; j < 4; ++j) hv[j] = x[j] * rs2 * Av[j] + Sv[j];
; #pragma unroll
;               for (int g = 0; g < 2; ++g) { u32x2 w; w.x = pk_fp8x4(hv[2 * g].x, hv[2 * g].y, hv[2 * g].z, hv[2 * g].w); w.y = pk_fp8x4(hv[2 * g + 1].x, hv[2 * g + 1].y, hv[2 * g + 1].z, hv[2 * g + 1].w);
;                   *(u32x2*)((unsigned char*)(F.ws + WS_H8) + (size_t)t * D + 8 * F.lane + 512 * g) = w; } }
; #pragma unroll
;             for (int g = 0; g < 2; ++g) { u32x4 w; w.x = pk2(hv[2 * g].x, hv[2 * g].y); w.y = pk2(hv[2 * g].z, hv[2 * g].w); w.z = pk2(hv[2 * g + 1].x, hv[2 * g + 1].y); w.w = pk2(hv[2 * g + 1].z, hv[2 * g + 1].w);
;                 *(LAS u32x4*)(Ht + tkl * HT_STRIDE + 8 * F.lane + 512 * g) = w; }
;         }
	v_lshrrev_b32_e32 v119, 16, v119
	v_add3_u32 v120, v107, v120, s15
	v_and_or_b32 v119, v120, s16, v119
	v_bfe_u32 v120, v114, 16, 1
	v_add3_u32 v120, v114, v120, s15
	v_bfe_u32 v121, v115, 16, 1
	v_lshrrev_b32_e32 v120, 16, v120
	v_add3_u32 v121, v115, v121, s15
	v_and_or_b32 v120, v121, s16, v120
	v_bfe_u32 v121, v108, 16, 1
	v_add3_u32 v121, v108, v121, s15
	v_lshrrev_b32_e32 v121, 16, v121
	v_and_or_b32 v121, v122, s16, v121
	global_store_dwordx4 v[116:117], v[118:121], off offset:1024
	v_pk_mul_f32 v[116:117], v[100:101], v[100:101]
	s_nop 0
	v_pk_mul_f32 v[118:119], v[102:103], v[102:103]
	s_nop 0
	v_pk_mov_b32 v[120:121], v[118:119], v[116:117] op_sel:[1,0]
	v_mov_b32_e32 v119, v117
	v_pk_add_f32 v[116:117], v[120:121], v[118:119]
	v_pk_mul_f32 v[118:119], v[104:105], v[104:105]
	v_pk_add_f32 v[116:117], v[116:117], v[116:117] op_sel_hi:[0,1]
	v_pk_mul_f32 v[120:121], v[110:111], v[110:111]
	v_mul_f32_e32 v116, v112, v112
	v_pk_mov_b32 v[122:123], v[120:121], v[118:119] op_sel:[1,0]
	v_mov_b32_e32 v121, v119
	v_pk_add_f32 v[118:119], v[122:123], v[120:121]
	v_pk_fma_f32 v[120:121], v[112:113], v[112:113], v[116:117] op_sel_hi:[1,1,0]
	v_mul_f32_e32 v116, v106, v106
	v_pk_add_f32 v[118:119], v[118:119], v[118:119] op_sel_hi:[0,1]
	v_pk_fma_f32 v[122:123], v[106:107], v[106:107], v[116:117] op_sel_hi:[1,1,0]
	v_mul_f32_e32 v120, v114, v114
	v_mul_f32_e32 v122, v115, v115
	v_mul_f32_e32 v116, v108, v108
	v_mul_f32_e32 v118, v109, v109
	v_pk_add_f32 v[120:121], v[120:121], v[122:123]
	v_pk_add_f32 v[116:117], v[116:117], v[118:119]
	s_nop 0
	v_pk_add_f32 v[116:117], v[120:121], v[116:117]
	s_nop 0
	v_add_f32_e32 v116, v116, v117
	s_nop 1
	v_add_f32_dpp v116, v116, v116 quad_perm:[1,0,3,2] row_mask:0xf bank_mask:0xf bound_ctrl:1
	s_nop 1
	v_add_f32_dpp v116, v116, v116 quad_perm:[2,3,0,1] row_mask:0xf bank_mask:0xf bound_ctrl:1
	s_nop 1
	v_add_f32_dpp v116, v116, v116 row_half_mirror row_mask:0xf bank_mask:0xf bound_ctrl:1
	s_nop 1
	v_add_f32_dpp v116, v116, v116 row_mirror row_mask:0xf bank_mask:0xf bound_ctrl:1
	s_nop 0
	v_readlane_b32 s2, v116, 16
	v_readlane_b32 s5, v116, 48
	v_readlane_b32 s6, v116, 0
	v_readlane_b32 s7, v116, 32
	v_mov_b32_e32 v116, s2
	v_mov_b32_e32 v117, s5
	v_pk_add_f32 v[116:117], s[6:7], v[116:117]
	s_nop 0
	v_add_f32_e32 v116, v116, v117
	v_mov_b32_e32 v117, 0x358637bd
	s_nop 0
	v_fmac_f32_e32 v117, 0x3a800000, v116
	v_rsq_f32_e32 v116, v117
	s_nop 0
	v_pk_mul_f32 v[102:103], v[102:103], v[116:117] op_sel_hi:[1,0]
	v_pk_mul_f32 v[100:101], v[100:101], v[116:117] op_sel_hi:[1,0]
	v_pk_mul_f32 v[104:105], v[104:105], v[116:117] op_sel_hi:[1,0]
	v_pk_fma_f32 v[118:119], v[84:85], v[100:101], v[6:7]
	v_pk_fma_f32 v[100:101], v[86:87], v[102:103], v[4:5]
	v_pk_mul_f32 v[102:103], v[110:111], v[116:117] op_sel_hi:[1,0]
	v_pk_mul_f32 v[110:111], v[112:113], v[116:117] op_sel_hi:[1,0]
	v_pk_fma_f32 v[102:103], v[90:91], v[102:103], v[0:1]
	v_pk_mul_f32 v[112:113], v[114:115], v[116:117] op_sel_hi:[1,0]
	v_mov_b32_e32 v114, v193
	v_mov_b32_e32 v115, v193
	v_cvt_pk_fp8_f32 v114, v100, v101
	v_cvt_pk_fp8_f32 v115, v102, v103
	v_pk_fma_f32 v[104:105], v[88:89], v[104:105], v[2:3]
	v_pk_mul_f32 v[106:107], v[106:107], v[116:117] op_sel_hi:[1,0]
	v_cvt_pk_fp8_f32 v114, v118, v119 op_sel:[0,0,1]
	v_cvt_pk_fp8_f32 v115, v104, v105 op_sel:[0,0,1]
	v_pk_mul_f32 v[108:109], v[108:109], v[116:117] op_sel_hi:[1,0]
	v_lshl_add_u64 v[116:117], v[60:61], 0, s[66:67]
	v_pk_fma_f32 v[110:111], v[94:95], v[110:111], v[12:13]
	v_pk_fma_f32 v[112:113], v[98:99], v[112:113], v[8:9]
	global_store_dwordx2 v[116:117], v[114:115], off
	v_mov_b32_e32 v114, v193
	v_mov_b32_e32 v115, v193
	v_cvt_pk_fp8_f32 v114, v110, v111
	v_cvt_pk_fp8_f32 v115, v112, v113
	v_pk_fma_f32 v[106:107], v[92:93], v[106:107], v[14:15]
	v_pk_fma_f32 v[108:109], v[96:97], v[108:109], v[10:11]
	v_cvt_pk_fp8_f32 v114, v106, v107 op_sel:[0,0,1]
	v_cvt_pk_fp8_f32 v115, v108, v109 op_sel:[0,0,1]
	v_lshl_add_u64 v[116:117], v[58:59], 0, s[66:67]
	v_add_co_u32_e32 v116, vcc, s18, v116
	s_nop 1
	v_addc_co_u32_e32 v117, vcc, 0, v117, vcc
	global_store_dwordx2 v[116:117], v[114:115], off offset:512
	v_bfe_u32 v114, v100, 16, 1
	v_add3_u32 v100, v100, v114, s15
	v_bfe_u32 v114, v101, 16, 1
	v_lshrrev_b32_e32 v100, 16, v100
	v_add3_u32 v101, v101, v114, s15
	v_and_or_b32 v100, v101, s16, v100
	v_bfe_u32 v101, v118, 16, 1
	v_add3_u32 v101, v118, v101, s15
	v_bfe_u32 v114, v119, 16, 1
	v_lshrrev_b32_e32 v101, 16, v101
	v_add3_u32 v114, v119, v114, s15
	v_and_or_b32 v101, v114, s16, v101
	v_bfe_u32 v114, v102, 16, 1
	v_add3_u32 v102, v102, v114, s15
	v_bfe_u32 v114, v103, 16, 1
	v_lshrrev_b32_e32 v102, 16, v102
	v_add3_u32 v103, v103, v114, s15
	v_and_or_b32 v102, v103, s16, v102
	v_bfe_u32 v103, v104, 16, 1
	v_add3_u32 v103, v104, v103, s15
	v_bfe_u32 v104, v105, 16, 1
	v_lshrrev_b32_e32 v103, 16, v103
	v_add3_u32 v104, v105, v104, s15
	v_and_or_b32 v103, v104, s16, v103
	ds_write_b128 v143, v[100:103] offset:2064
	v_bfe_u32 v100, v110, 16, 1
	v_add3_u32 v100, v110, v100, s15
	v_bfe_u32 v101, v111, 16, 1
	v_lshrrev_b32_e32 v100, 16, v100
	v_add3_u32 v101, v111, v101, s15
	v_and_or_b32 v100, v101, s16, v100
	v_bfe_u32 v101, v106, 16, 1
	v_add3_u32 v101, v106, v101, s15
	v_bfe_u32 v102, v107, 16, 1
	v_lshrrev_b32_e32 v101, 16, v101
	v_add3_u32 v102, v107, v102, s15
	v_and_or_b32 v101, v102, s16, v101
	v_bfe_u32 v102, v112, 16, 1
	v_add3_u32 v102, v112, v102, s15
	v_bfe_u32 v103, v113, 16, 1
	v_lshrrev_b32_e32 v102, 16, v102
	v_add3_u32 v103, v113, v103, s15
	v_and_or_b32 v102, v103, s16, v102
	v_bfe_u32 v103, v108, 16, 1
	v_add3_u32 v103, v108, v103, s15
	v_bfe_u32 v104, v109, 16, 1
	v_lshrrev_b32_e32 v103, 16, v103
	v_add3_u32 v104, v109, v104, s15
	v_and_or_b32 v103, v104, s16, v103
	ds_write_b128 v143, v[100:103] offset:3088
	s_cbranch_scc0 .LBB0_960
; #define LAS __attribute__((address_space(3)))
; DI void phase_tail(const Frame& F, int l) {
;     ...
;         __syncthreads();
;         { f32x16 acc;
; #pragma unroll
;           for (int i = 0; i < 16; ++i) acc[i] = 0.f;
; #pragma unroll
;           for (int s = 0; s < 8; ++s) { const bf16x8 af = *(const LAS bf16x8*)(Ht + r * HT_STRIDE + 128 * F.wave + 16 * s + 8 * h);
;               acc = __builtin_amdgcn_mfma_f32_32x32x16_bf16(af, RWf[s], acc, 0, 0, 0); }
; #pragma unroll
;           for (int i = 0; i < 16; ++i) Pz[(F.wave * 32 + ((i & 3) + 8 * (i >> 2) + 4 * h)) * 32 + r] = acc[i]; }
;         __syncthreads();
	s_waitcnt lgkmcnt(0)
	s_barrier
	ds_read_b128 v[0:3], v141
	ds_read_b128 v[62:65], v141 offset:32
	s_lshl_b32 s10, s24, 5
	s_mov_b32 s2, 0
	s_mov_b64 s[66:67], -1
	v_add_u32_e32 v68, 0x400, v142
	s_waitcnt lgkmcnt(1)
	v_mfma_f32_32x32x16_bf16 v[0:15], v[0:3], v[16:19], 0
	v_add_u32_e32 v69, 0x800, v142
	v_add_u32_e32 v70, 0xc00, v142
	s_waitcnt lgkmcnt(0)
	v_mfma_f32_32x32x16_bf16 v[0:15], v[62:65], v[20:23], v[0:15]
	ds_read_b128 v[62:65], v141 offset:64
	s_waitcnt lgkmcnt(0)
	v_mfma_f32_32x32x16_bf16 v[0:15], v[62:65], v[24:27], v[0:15]
	ds_read_b128 v[62:65], v141 offset:96
	s_waitcnt lgkmcnt(0)
	v_mfma_f32_32x32x16_bf16 v[0:15], v[62:65], v[28:31], v[0:15]
	ds_read_b128 v[62:65], v141 offset:128
	s_waitcnt lgkmcnt(0)
	v_mfma_f32_32x32x16_bf16 v[0:15], v[62:65], v[32:35], v[0:15]
	ds_read_b128 v[62:65], v141 offset:160
	s_waitcnt lgkmcnt(0)
	v_mfma_f32_32x32x16_bf16 v[0:15], v[62:65], v[36:39], v[0:15]
	ds_read_b128 v[62:65], v141 offset:192
	s_waitcnt lgkmcnt(0)
	v_mfma_f32_32x32x16_bf16 v[0:15], v[62:65], v[40:43], v[0:15]
	ds_read_b128 v[62:65], v141 offset:224
	s_waitcnt lgkmcnt(0)
	v_mfma_f32_32x32x16_bf16 v[0:15], v[62:65], v[44:47], v[0:15]
	s_nop 11
	ds_write2_b32 v142, v0, v1 offset1:32
	ds_write2_b32 v142, v2, v3 offset0:64 offset1:96
	ds_write2_b32 v68, v4, v5 offset1:32
	ds_write2_b32 v68, v6, v7 offset0:64 offset1:96
	ds_write2_b32 v69, v8, v9 offset1:32
	ds_write2_b32 v69, v10, v11 offset0:64 offset1:96
	ds_write2_b32 v70, v12, v13 offset1:32
	ds_write2_b32 v70, v14, v15 offset0:64 offset1:96
	s_waitcnt lgkmcnt(0)
	s_barrier
	s_branch .LBB0_963
